# all three GEMM kernels: K-loops merged to 4 barrier-phases per 2 K-tiles (32 MFMA per phase), prologue vmcnt(2)
# speedup vs baseline: 1.0165x; 1.0125x over previous
.LBB4_2:
	s_or_b64 exec, exec, s[4:5]
	s_add_i32 s24, s16, 1
	s_ashr_i32 s25, s24, 31
	s_lshl_b64 s[4:5], s[24:25], 7
	s_add_u32 s20, s6, s4
	s_addc_u32 s21, s7, s5
	s_add_i32 s39, 0, 0x18000
	v_add_u32_e32 v154, s39, v2
	v_lshl_add_u64 v[4:5], s[20:21], 0, v[138:139]
	v_readfirstlane_b32 s43, v154
	s_mov_b32 m0, s43
	v_add_u32_e32 v6, 0x2000, v154
	s_waitcnt vmcnt(2)
	s_barrier
	global_load_lds_dwordx4 v[4:5], off
	v_lshl_add_u64 v[4:5], s[20:21], 0, v[140:141]
	v_readfirstlane_b32 s20, v6
	s_mov_b32 m0, s20
	s_add_u32 s20, s8, s4
	s_addc_u32 s21, s9, s5
	v_add_u32_e32 v6, 0x8000, v1
	s_add_u32 s4, s10, s4
	v_readfirstlane_b32 s43, v6
	global_load_lds_dwordx4 v[4:5], off
	v_lshl_add_u64 v[4:5], v[134:135], 1, s[20:21]
	s_mov_b32 m0, s43
	v_add_u32_e32 v6, 0xa000, v1
	s_addc_u32 s5, s11, s5
	s_add_i32 s43, 0, 0x1c000
	global_load_lds_dwordx4 v[4:5], off
	v_lshl_add_u64 v[4:5], v[136:137], 1, s[20:21]
	v_readfirstlane_b32 s20, v6
	v_add_u32_e32 v155, s43, v2
	s_mov_b32 m0, s20
	v_readfirstlane_b32 s20, v155
	global_load_lds_dwordx4 v[4:5], off
	v_lshl_add_u64 v[4:5], s[4:5], 0, v[138:139]
	s_mov_b32 m0, s20
	v_add_u32_e32 v2, 0x2000, v155
	global_load_lds_dwordx4 v[4:5], off
	v_lshl_add_u64 v[4:5], s[4:5], 0, v[140:141]
	v_readfirstlane_b32 s4, v2
	s_mov_b32 m0, s4
	s_cmp_gt_i32 s19, 2
	global_load_lds_dwordx4 v[4:5], off
	v_lshlrev_b32_e32 v4, 6, v0
	v_lshlrev_b32_e32 v5, 2, v0
	s_waitcnt vmcnt(6)
	v_and_b32_e32 v161, 48, v0
	v_and_b32_e32 v4, 0x3c0, v4
	v_and_b32_e32 v5, 32, v5
	v_bfe_u32 v147, v0, 6, 2
	s_cselect_b64 s[20:21], -1, 0
	v_bitop3_b32 v4, v4, v5, v161 bitop3:0x36
	v_lshlrev_b32_e32 v163, 6, v3
	v_and_b32_e32 v162, 15, v0
	v_lshlrev_b32_e32 v2, 12, v147
	v_add_u32_e32 v5, s36, v4
	v_add_u32_e32 v6, s38, v4
	v_add_u32_e32 v7, s39, v4
	v_add_u32_e32 v8, s43, v4
	s_and_b64 vcc, exec, s[20:21]
	v_lshlrev_b32_e32 v157, 13, v3
	v_or_b32_e32 v166, 16, v163
	v_or_b32_e32 v165, 32, v163
	v_or_b32_e32 v164, 48, v163
	s_barrier
	s_cbranch_vccnz .LBB4_4
	v_lshlrev_b32_e32 v158, 13, v3
	v_or_b32_e32 v3, v166, v162
	v_lshlrev_b32_e32 v9, 6, v3
	v_lshlrev_b32_e32 v3, 2, v3
	v_and_b32_e32 v9, 0x3c0, v9
	v_and_b32_e32 v3, 32, v3
	v_bitop3_b32 v130, v9, v3, v161 bitop3:0x36
	v_or_b32_e32 v3, v165, v162
	v_lshlrev_b32_e32 v9, 6, v3
	v_lshlrev_b32_e32 v3, 2, v3
	v_and_b32_e32 v9, 0x3c0, v9
	v_and_b32_e32 v3, 32, v3
	v_bitop3_b32 v132, v9, v3, v161 bitop3:0x36
	v_or_b32_e32 v3, v164, v162
	v_lshlrev_b32_e32 v9, 6, v3
	v_lshlrev_b32_e32 v3, 2, v3
	v_and_b32_e32 v9, 0x3c0, v9
	v_and_b32_e32 v3, 32, v3
	v_lshlrev_b32_e32 v131, 7, v166
	v_lshlrev_b32_e32 v133, 7, v165
	v_bitop3_b32 v159, v9, v3, v161 bitop3:0x36
	v_lshlrev_b32_e32 v160, 7, v164
	s_mov_b64 s[4:5], 0
	s_branch .LBB4_5

.LBB4_7:
	ds_read_b128 v[178:181], v151
	ds_read_b128 v[182:185], v151 offset:1024
	ds_read_b128 v[186:189], v151 offset:2048
	ds_read_b128 v[190:193], v151 offset:3072
	s_add_i32 s39, s16, s38
	s_add_i32 s4, s39, 1
	s_ashr_i32 s5, s4, 31
	s_lshl_b64 s[4:5], s[4:5], 7
	s_add_u32 s4, s26, s4
	s_addc_u32 s5, s27, s5
	v_readfirstlane_b32 s43, v166
	v_lshl_add_u64 v[194:195], s[4:5], 0, v[142:143]
	s_mov_b32 m0, s43
	s_nop 0
	global_load_lds_dwordx4 v[194:195], off
	v_lshl_add_u64 v[194:195], s[4:5], 0, v[144:145]
	v_readfirstlane_b32 s4, v167
	s_mov_b32 m0, s4
	s_nop 0
	global_load_lds_dwordx4 v[194:195], off
	ds_read_b128 v[194:197], v158
	ds_read_b128 v[198:201], v158 offset:1024
	ds_read_b128 v[202:205], v161
	ds_read_b128 v[206:209], v161 offset:1024
	ds_read_b128 v[210:213], v164
	ds_read_b128 v[214:217], v164 offset:1024
	ds_read_b128 v[218:221], v165
	ds_read_b128 v[222:225], v165 offset:1024
	ds_read_b128 v[226:229], v150
	ds_read_b128 v[230:233], v150 offset:1024
	ds_read_b128 v[234:237], v150 offset:2048
	ds_read_b128 v[238:241], v150 offset:3072
	s_waitcnt lgkmcnt(0)
	s_barrier
	s_setprio 1
	v_mfma_f32_16x16x32_f16 v[110:113], v[178:181], v[194:197], v[110:113]
	v_mfma_f32_16x16x32_f16 v[126:129], v[186:189], v[194:197], v[126:129]
	v_mfma_f32_16x16x32_f16 v[122:125], v[178:181], v[202:205], v[122:125]
	v_mfma_f32_16x16x32_f16 v[118:121], v[186:189], v[202:205], v[118:121]
	v_mfma_f32_16x16x32_f16 v[114:117], v[178:181], v[210:213], v[114:117]
	v_mfma_f32_16x16x32_f16 v[106:109], v[186:189], v[210:213], v[106:109]
	v_mfma_f32_16x16x32_f16 v[102:105], v[178:181], v[218:221], v[102:105]
	v_mfma_f32_16x16x32_f16 v[98:101], v[186:189], v[218:221], v[98:101]
	v_mfma_f32_16x16x32_f16 v[110:113], v[182:185], v[198:201], v[110:113]
	v_mfma_f32_16x16x32_f16 v[126:129], v[190:193], v[198:201], v[126:129]
	v_mfma_f32_16x16x32_f16 v[122:125], v[182:185], v[206:209], v[122:125]
	v_mfma_f32_16x16x32_f16 v[118:121], v[190:193], v[206:209], v[118:121]
	v_mfma_f32_16x16x32_f16 v[114:117], v[182:185], v[214:217], v[114:117]
	v_mfma_f32_16x16x32_f16 v[106:109], v[190:193], v[214:217], v[106:109]
	v_mfma_f32_16x16x32_f16 v[102:105], v[182:185], v[222:225], v[102:105]
	v_mfma_f32_16x16x32_f16 v[98:101], v[190:193], v[222:225], v[98:101]
	v_mfma_f32_16x16x32_f16 v[94:97], v[226:229], v[194:197], v[94:97]
	v_mfma_f32_16x16x32_f16 v[90:93], v[234:237], v[194:197], v[90:93]
	v_mfma_f32_16x16x32_f16 v[86:89], v[226:229], v[202:205], v[86:89]
	v_mfma_f32_16x16x32_f16 v[82:85], v[234:237], v[202:205], v[82:85]
	v_mfma_f32_16x16x32_f16 v[78:81], v[226:229], v[210:213], v[78:81]
	v_mfma_f32_16x16x32_f16 v[74:77], v[234:237], v[210:213], v[74:77]
	v_mfma_f32_16x16x32_f16 v[70:73], v[226:229], v[218:221], v[70:73]
	v_mfma_f32_16x16x32_f16 v[66:69], v[234:237], v[218:221], v[66:69]
	v_mfma_f32_16x16x32_f16 v[94:97], v[230:233], v[198:201], v[94:97]
	v_mfma_f32_16x16x32_f16 v[90:93], v[238:241], v[198:201], v[90:93]
	v_mfma_f32_16x16x32_f16 v[86:89], v[230:233], v[206:209], v[86:89]
	v_mfma_f32_16x16x32_f16 v[82:85], v[238:241], v[206:209], v[82:85]
	v_mfma_f32_16x16x32_f16 v[78:81], v[230:233], v[214:217], v[78:81]
	v_mfma_f32_16x16x32_f16 v[74:77], v[238:241], v[214:217], v[74:77]
	v_mfma_f32_16x16x32_f16 v[70:73], v[230:233], v[222:225], v[70:73]
	v_mfma_f32_16x16x32_f16 v[66:69], v[238:241], v[222:225], v[66:69]
	s_setprio 0
	s_barrier
	ds_read_b128 v[194:197], v158 offset:16384
	ds_read_b128 v[198:201], v158 offset:17408
	ds_read_b128 v[202:205], v161 offset:16384
	ds_read_b128 v[206:209], v161 offset:17408
	ds_read_b128 v[210:213], v164 offset:16384
	ds_read_b128 v[214:217], v164 offset:17408
	ds_read_b128 v[218:221], v165 offset:16384
	ds_read_b128 v[222:225], v165 offset:17408
	s_add_i32 s4, s39, 2
	s_ashr_i32 s5, s4, 31
	s_add_i32 s38, s38, 2
	s_lshl_b64 s[4:5], s[4:5], 7
	s_add_u32 s44, s6, s4
	s_addc_u32 s45, s7, s5
	v_readfirstlane_b32 s43, v152
	v_lshl_add_u64 v[242:243], s[44:45], 0, v[138:139]
	s_mov_b32 m0, s43
	v_readfirstlane_b32 s43, v168
	global_load_lds_dwordx4 v[242:243], off
	v_lshl_add_u64 v[242:243], s[44:45], 0, v[140:141]
	s_mov_b32 m0, s43
	s_nop 0
	global_load_lds_dwordx4 v[242:243], off
	s_add_u32 s44, s8, s4
	s_addc_u32 s45, s9, s5
	v_readfirstlane_b32 s43, v1
	v_lshl_add_u64 v[242:243], s[44:45], 0, v[142:143]
	s_mov_b32 m0, s43
	v_readfirstlane_b32 s43, v169
	global_load_lds_dwordx4 v[242:243], off
	v_lshl_add_u64 v[242:243], s[44:45], 0, v[144:145]
	s_mov_b32 m0, s43
	s_nop 0
	global_load_lds_dwordx4 v[242:243], off
	s_add_u32 s44, s10, s4
	s_addc_u32 s45, s11, s5
	v_readfirstlane_b32 s43, v153
	v_lshl_add_u64 v[242:243], s[44:45], 0, v[138:139]
	s_mov_b32 m0, s43
	v_readfirstlane_b32 s43, v170
	global_load_lds_dwordx4 v[242:243], off
	v_lshl_add_u64 v[242:243], s[44:45], 0, v[140:141]
	s_mov_b32 m0, s43
	s_nop 0
	global_load_lds_dwordx4 v[242:243], off
	s_waitcnt vmcnt(6)
	s_waitcnt lgkmcnt(0)
	s_barrier
	s_setprio 1
	v_mfma_f32_16x16x32_f16 v[62:65], v[178:181], v[194:197], v[62:65]
	v_mfma_f32_16x16x32_f16 v[58:61], v[186:189], v[194:197], v[58:61]
	v_mfma_f32_16x16x32_f16 v[54:57], v[178:181], v[202:205], v[54:57]
	v_mfma_f32_16x16x32_f16 v[50:53], v[186:189], v[202:205], v[50:53]
	v_mfma_f32_16x16x32_f16 v[46:49], v[178:181], v[210:213], v[46:49]
	v_mfma_f32_16x16x32_f16 v[42:45], v[186:189], v[210:213], v[42:45]
	v_mfma_f32_16x16x32_f16 v[38:41], v[178:181], v[218:221], v[38:41]
	v_mfma_f32_16x16x32_f16 v[34:37], v[186:189], v[218:221], v[34:37]
	v_mfma_f32_16x16x32_f16 v[62:65], v[182:185], v[198:201], v[62:65]
	v_mfma_f32_16x16x32_f16 v[58:61], v[190:193], v[198:201], v[58:61]
	v_mfma_f32_16x16x32_f16 v[54:57], v[182:185], v[206:209], v[54:57]
	v_mfma_f32_16x16x32_f16 v[50:53], v[190:193], v[206:209], v[50:53]
	v_mfma_f32_16x16x32_f16 v[46:49], v[182:185], v[214:217], v[46:49]
	v_mfma_f32_16x16x32_f16 v[42:45], v[190:193], v[214:217], v[42:45]
	v_mfma_f32_16x16x32_f16 v[38:41], v[182:185], v[222:225], v[38:41]
	v_mfma_f32_16x16x32_f16 v[34:37], v[190:193], v[222:225], v[34:37]
	v_mfma_f32_16x16x32_f16 v[30:33], v[226:229], v[194:197], v[30:33]
	v_mfma_f32_16x16x32_f16 v[26:29], v[234:237], v[194:197], v[26:29]
	v_mfma_f32_16x16x32_f16 v[22:25], v[226:229], v[202:205], v[22:25]
	v_mfma_f32_16x16x32_f16 v[18:21], v[234:237], v[202:205], v[18:21]
	v_mfma_f32_16x16x32_f16 v[14:17], v[226:229], v[210:213], v[14:17]
	v_mfma_f32_16x16x32_f16 v[10:13], v[234:237], v[210:213], v[10:13]
	v_mfma_f32_16x16x32_f16 v[6:9], v[226:229], v[218:221], v[6:9]
	v_mfma_f32_16x16x32_f16 v[2:5], v[234:237], v[218:221], v[2:5]
	v_mfma_f32_16x16x32_f16 v[30:33], v[230:233], v[198:201], v[30:33]
	v_mfma_f32_16x16x32_f16 v[26:29], v[238:241], v[198:201], v[26:29]
	v_mfma_f32_16x16x32_f16 v[22:25], v[230:233], v[206:209], v[22:25]
	v_mfma_f32_16x16x32_f16 v[18:21], v[238:241], v[206:209], v[18:21]
	v_mfma_f32_16x16x32_f16 v[14:17], v[230:233], v[214:217], v[14:17]
	v_mfma_f32_16x16x32_f16 v[10:13], v[238:241], v[214:217], v[10:13]
	v_mfma_f32_16x16x32_f16 v[6:9], v[230:233], v[222:225], v[6:9]
	v_mfma_f32_16x16x32_f16 v[2:5], v[238:241], v[222:225], v[2:5]
	s_setprio 0
	s_barrier
	ds_read_b128 v[178:181], v149
	ds_read_b128 v[182:185], v149 offset:1024
	ds_read_b128 v[186:189], v149 offset:2048
	ds_read_b128 v[190:193], v149 offset:3072
	s_add_u32 s4, s26, s4
	s_addc_u32 s5, s27, s5
	v_readfirstlane_b32 s43, v171
	v_lshl_add_u64 v[226:227], s[4:5], 0, v[142:143]
	s_mov_b32 m0, s43
	ds_read_b128 v[194:197], v158 offset:32768
	ds_read_b128 v[198:201], v158 offset:33792
	ds_read_b128 v[202:205], v161 offset:32768
	ds_read_b128 v[206:209], v161 offset:33792
	ds_read_b128 v[210:213], v164 offset:32768
	ds_read_b128 v[214:217], v164 offset:33792
	ds_read_b128 v[218:221], v165 offset:32768
	ds_read_b128 v[222:225], v165 offset:33792
	global_load_lds_dwordx4 v[226:227], off
	v_lshl_add_u64 v[226:227], s[4:5], 0, v[144:145]
	v_readfirstlane_b32 s4, v172
	s_mov_b32 m0, s4
	s_nop 0
	global_load_lds_dwordx4 v[226:227], off
	ds_read_b128 v[226:229], v148
	ds_read_b128 v[230:233], v148 offset:1024
	ds_read_b128 v[234:237], v148 offset:2048
	ds_read_b128 v[238:241], v148 offset:3072
	s_waitcnt lgkmcnt(0)
	s_barrier
	s_setprio 1
	v_mfma_f32_16x16x32_f16 v[110:113], v[178:181], v[194:197], v[110:113]
	v_mfma_f32_16x16x32_f16 v[126:129], v[186:189], v[194:197], v[126:129]
	v_mfma_f32_16x16x32_f16 v[122:125], v[178:181], v[202:205], v[122:125]
	v_mfma_f32_16x16x32_f16 v[118:121], v[186:189], v[202:205], v[118:121]
	v_mfma_f32_16x16x32_f16 v[114:117], v[178:181], v[210:213], v[114:117]
	v_mfma_f32_16x16x32_f16 v[106:109], v[186:189], v[210:213], v[106:109]
	v_mfma_f32_16x16x32_f16 v[102:105], v[178:181], v[218:221], v[102:105]
	v_mfma_f32_16x16x32_f16 v[98:101], v[186:189], v[218:221], v[98:101]
	v_mfma_f32_16x16x32_f16 v[110:113], v[182:185], v[198:201], v[110:113]
	v_mfma_f32_16x16x32_f16 v[126:129], v[190:193], v[198:201], v[126:129]
	v_mfma_f32_16x16x32_f16 v[122:125], v[182:185], v[206:209], v[122:125]
	v_mfma_f32_16x16x32_f16 v[118:121], v[190:193], v[206:209], v[118:121]
	v_mfma_f32_16x16x32_f16 v[114:117], v[182:185], v[214:217], v[114:117]
	v_mfma_f32_16x16x32_f16 v[106:109], v[190:193], v[214:217], v[106:109]
	v_mfma_f32_16x16x32_f16 v[102:105], v[182:185], v[222:225], v[102:105]
	v_mfma_f32_16x16x32_f16 v[98:101], v[190:193], v[222:225], v[98:101]
	v_mfma_f32_16x16x32_f16 v[94:97], v[226:229], v[194:197], v[94:97]
	v_mfma_f32_16x16x32_f16 v[90:93], v[234:237], v[194:197], v[90:93]
	v_mfma_f32_16x16x32_f16 v[86:89], v[226:229], v[202:205], v[86:89]
	v_mfma_f32_16x16x32_f16 v[82:85], v[234:237], v[202:205], v[82:85]
	v_mfma_f32_16x16x32_f16 v[78:81], v[226:229], v[210:213], v[78:81]
	v_mfma_f32_16x16x32_f16 v[74:77], v[234:237], v[210:213], v[74:77]
	v_mfma_f32_16x16x32_f16 v[70:73], v[226:229], v[218:221], v[70:73]
	v_mfma_f32_16x16x32_f16 v[66:69], v[234:237], v[218:221], v[66:69]
	v_mfma_f32_16x16x32_f16 v[94:97], v[230:233], v[198:201], v[94:97]
	v_mfma_f32_16x16x32_f16 v[90:93], v[238:241], v[198:201], v[90:93]
	v_mfma_f32_16x16x32_f16 v[86:89], v[230:233], v[206:209], v[86:89]
	v_mfma_f32_16x16x32_f16 v[82:85], v[238:241], v[206:209], v[82:85]
	v_mfma_f32_16x16x32_f16 v[78:81], v[230:233], v[214:217], v[78:81]
	v_mfma_f32_16x16x32_f16 v[74:77], v[238:241], v[214:217], v[74:77]
	v_mfma_f32_16x16x32_f16 v[70:73], v[230:233], v[222:225], v[70:73]
	v_mfma_f32_16x16x32_f16 v[66:69], v[238:241], v[222:225], v[66:69]
	s_setprio 0
	s_barrier
	ds_read_b128 v[194:197], v158 offset:49152
	ds_read_b128 v[198:201], v158 offset:50176
	ds_read_b128 v[202:205], v161 offset:49152
	ds_read_b128 v[206:209], v161 offset:50176
	ds_read_b128 v[210:213], v164 offset:49152
	ds_read_b128 v[214:217], v164 offset:50176
	ds_read_b128 v[218:221], v165 offset:49152
	ds_read_b128 v[222:225], v165 offset:50176
	s_add_i32 s4, s39, 3
	s_ashr_i32 s5, s4, 31
	s_lshl_b64 s[4:5], s[4:5], 7
	s_add_u32 s44, s6, s4
	s_addc_u32 s45, s7, s5
	v_readfirstlane_b32 s39, v154
	v_lshl_add_u64 v[242:243], s[44:45], 0, v[138:139]
	s_mov_b32 m0, s39
	v_readfirstlane_b32 s39, v173
	global_load_lds_dwordx4 v[242:243], off
	v_lshl_add_u64 v[242:243], s[44:45], 0, v[140:141]
	s_mov_b32 m0, s39
	s_nop 0
	global_load_lds_dwordx4 v[242:243], off
	s_add_u32 s44, s8, s4
	s_addc_u32 s45, s9, s5
	v_readfirstlane_b32 s39, v174
	v_lshl_add_u64 v[242:243], s[44:45], 0, v[142:143]
	s_mov_b32 m0, s39
	v_readfirstlane_b32 s39, v175
	global_load_lds_dwordx4 v[242:243], off
	v_lshl_add_u64 v[242:243], s[44:45], 0, v[144:145]
	s_mov_b32 m0, s39
	s_nop 0
	global_load_lds_dwordx4 v[242:243], off
	s_add_u32 s4, s10, s4
	s_addc_u32 s5, s11, s5
	v_readfirstlane_b32 s39, v155
	v_lshl_add_u64 v[242:243], s[4:5], 0, v[138:139]
	s_mov_b32 m0, s39
	s_nop 0
	global_load_lds_dwordx4 v[242:243], off
	v_lshl_add_u64 v[242:243], s[4:5], 0, v[140:141]
	v_readfirstlane_b32 s4, v176
	s_mov_b32 m0, s4
	s_nop 0
	global_load_lds_dwordx4 v[242:243], off
	s_waitcnt vmcnt(6)
	s_waitcnt lgkmcnt(0)
	s_barrier
	s_setprio 1
	v_mfma_f32_16x16x32_f16 v[62:65], v[178:181], v[194:197], v[62:65]
	v_mfma_f32_16x16x32_f16 v[58:61], v[186:189], v[194:197], v[58:61]
	v_mfma_f32_16x16x32_f16 v[54:57], v[178:181], v[202:205], v[54:57]
	v_mfma_f32_16x16x32_f16 v[50:53], v[186:189], v[202:205], v[50:53]
	v_mfma_f32_16x16x32_f16 v[46:49], v[178:181], v[210:213], v[46:49]
	v_mfma_f32_16x16x32_f16 v[42:45], v[186:189], v[210:213], v[42:45]
	v_mfma_f32_16x16x32_f16 v[38:41], v[178:181], v[218:221], v[38:41]
	v_mfma_f32_16x16x32_f16 v[34:37], v[186:189], v[218:221], v[34:37]
	v_mfma_f32_16x16x32_f16 v[62:65], v[182:185], v[198:201], v[62:65]
	v_mfma_f32_16x16x32_f16 v[58:61], v[190:193], v[198:201], v[58:61]
	v_mfma_f32_16x16x32_f16 v[54:57], v[182:185], v[206:209], v[54:57]
	v_mfma_f32_16x16x32_f16 v[50:53], v[190:193], v[206:209], v[50:53]
	v_mfma_f32_16x16x32_f16 v[46:49], v[182:185], v[214:217], v[46:49]
	v_mfma_f32_16x16x32_f16 v[42:45], v[190:193], v[214:217], v[42:45]
	v_mfma_f32_16x16x32_f16 v[38:41], v[182:185], v[222:225], v[38:41]
	v_mfma_f32_16x16x32_f16 v[34:37], v[190:193], v[222:225], v[34:37]
	v_mfma_f32_16x16x32_f16 v[30:33], v[226:229], v[194:197], v[30:33]
	v_mfma_f32_16x16x32_f16 v[26:29], v[234:237], v[194:197], v[26:29]
	v_mfma_f32_16x16x32_f16 v[22:25], v[226:229], v[202:205], v[22:25]
	v_mfma_f32_16x16x32_f16 v[18:21], v[234:237], v[202:205], v[18:21]
	v_mfma_f32_16x16x32_f16 v[14:17], v[226:229], v[210:213], v[14:17]
	v_mfma_f32_16x16x32_f16 v[10:13], v[234:237], v[210:213], v[10:13]
	v_mfma_f32_16x16x32_f16 v[6:9], v[226:229], v[218:221], v[6:9]
	v_mfma_f32_16x16x32_f16 v[2:5], v[234:237], v[218:221], v[2:5]
	v_mfma_f32_16x16x32_f16 v[30:33], v[230:233], v[198:201], v[30:33]
	v_mfma_f32_16x16x32_f16 v[26:29], v[238:241], v[198:201], v[26:29]
	v_mfma_f32_16x16x32_f16 v[22:25], v[230:233], v[206:209], v[22:25]
	v_mfma_f32_16x16x32_f16 v[18:21], v[238:241], v[206:209], v[18:21]
	v_mfma_f32_16x16x32_f16 v[14:17], v[230:233], v[214:217], v[14:17]
	v_mfma_f32_16x16x32_f16 v[10:13], v[238:241], v[214:217], v[10:13]
	v_mfma_f32_16x16x32_f16 v[6:9], v[230:233], v[222:225], v[6:9]
	v_mfma_f32_16x16x32_f16 v[2:5], v[238:241], v[222:225], v[2:5]
	s_setprio 0
	s_cmp_lt_i32 s38, s36
	s_barrier
	s_cbranch_scc1 .LBB4_7
	v_mov_b32_e32 v158, v157

.LBB4_203:
	ds_read_b128 v[168:171], v151
	ds_read_b128 v[172:175], v151 offset:1024
	ds_read_b128 v[176:179], v151 offset:2048
	ds_read_b128 v[180:183], v151 offset:3072
	s_add_i32 s23, s16, s22
	s_add_i32 s0, s23, 1
	s_ashr_i32 s1, s0, 31
	s_lshl_b64 s[0:1], s[0:1], 7
	s_add_u32 s0, s2, s0
	s_addc_u32 s1, s3, s1
	v_readfirstlane_b32 s24, v130
	v_lshl_add_u64 v[216:217], s[0:1], 0, v[142:143]
	s_mov_b32 m0, s24
	ds_read_b128 v[184:187], v156
	ds_read_b128 v[188:191], v156 offset:1024
	ds_read_b128 v[192:195], v157
	ds_read_b128 v[196:199], v157 offset:1024
	ds_read_b128 v[200:203], v158
	ds_read_b128 v[204:207], v158 offset:1024
	ds_read_b128 v[208:211], v159
	ds_read_b128 v[212:215], v159 offset:1024
	global_load_lds_dwordx4 v[216:217], off
	v_lshl_add_u64 v[216:217], s[0:1], 0, v[144:145]
	v_readfirstlane_b32 s0, v131
	s_mov_b32 m0, s0
	s_nop 0
	global_load_lds_dwordx4 v[216:217], off
	ds_read_b128 v[216:219], v150
	ds_read_b128 v[220:223], v150 offset:1024
	ds_read_b128 v[224:227], v150 offset:2048
	ds_read_b128 v[228:231], v150 offset:3072
	s_waitcnt lgkmcnt(0)
	s_barrier
	s_setprio 1
	v_mfma_f32_16x16x32_f16 v[2:5], v[168:171], v[184:187], v[2:5]
	v_mfma_f32_16x16x32_f16 v[126:129], v[176:179], v[184:187], v[126:129]
	v_mfma_f32_16x16x32_f16 v[122:125], v[168:171], v[192:195], v[122:125]
	v_mfma_f32_16x16x32_f16 v[118:121], v[176:179], v[192:195], v[118:121]
	v_mfma_f32_16x16x32_f16 v[114:117], v[168:171], v[200:203], v[114:117]
	v_mfma_f32_16x16x32_f16 v[110:113], v[176:179], v[200:203], v[110:113]
	v_mfma_f32_16x16x32_f16 v[106:109], v[168:171], v[208:211], v[106:109]
	v_mfma_f32_16x16x32_f16 v[102:105], v[176:179], v[208:211], v[102:105]
	v_mfma_f32_16x16x32_f16 v[2:5], v[172:175], v[188:191], v[2:5]
	v_mfma_f32_16x16x32_f16 v[126:129], v[180:183], v[188:191], v[126:129]
	v_mfma_f32_16x16x32_f16 v[122:125], v[172:175], v[196:199], v[122:125]
	v_mfma_f32_16x16x32_f16 v[118:121], v[180:183], v[196:199], v[118:121]
	v_mfma_f32_16x16x32_f16 v[114:117], v[172:175], v[204:207], v[114:117]
	v_mfma_f32_16x16x32_f16 v[110:113], v[180:183], v[204:207], v[110:113]
	v_mfma_f32_16x16x32_f16 v[106:109], v[172:175], v[212:215], v[106:109]
	v_mfma_f32_16x16x32_f16 v[102:105], v[180:183], v[212:215], v[102:105]
	v_mfma_f32_16x16x32_f16 v[98:101], v[216:219], v[184:187], v[98:101]
	v_mfma_f32_16x16x32_f16 v[94:97], v[224:227], v[184:187], v[94:97]
	v_mfma_f32_16x16x32_f16 v[90:93], v[216:219], v[192:195], v[90:93]
	v_mfma_f32_16x16x32_f16 v[86:89], v[224:227], v[192:195], v[86:89]
	v_mfma_f32_16x16x32_f16 v[82:85], v[216:219], v[200:203], v[82:85]
	v_mfma_f32_16x16x32_f16 v[78:81], v[224:227], v[200:203], v[78:81]
	v_mfma_f32_16x16x32_f16 v[74:77], v[216:219], v[208:211], v[74:77]
	v_mfma_f32_16x16x32_f16 v[70:73], v[224:227], v[208:211], v[70:73]
	v_mfma_f32_16x16x32_f16 v[98:101], v[220:223], v[188:191], v[98:101]
	v_mfma_f32_16x16x32_f16 v[94:97], v[228:231], v[188:191], v[94:97]
	v_mfma_f32_16x16x32_f16 v[90:93], v[220:223], v[196:199], v[90:93]
	v_mfma_f32_16x16x32_f16 v[86:89], v[228:231], v[196:199], v[86:89]
	v_mfma_f32_16x16x32_f16 v[82:85], v[220:223], v[204:207], v[82:85]
	v_mfma_f32_16x16x32_f16 v[78:81], v[228:231], v[204:207], v[78:81]
	v_mfma_f32_16x16x32_f16 v[74:77], v[220:223], v[212:215], v[74:77]
	v_mfma_f32_16x16x32_f16 v[70:73], v[228:231], v[212:215], v[70:73]
	s_setprio 0
	s_barrier
	ds_read_b128 v[184:187], v156 offset:16384
	ds_read_b128 v[188:191], v156 offset:17408
	ds_read_b128 v[192:195], v157 offset:16384
	ds_read_b128 v[196:199], v157 offset:17408
	ds_read_b128 v[200:203], v158 offset:16384
	ds_read_b128 v[204:207], v158 offset:17408
	ds_read_b128 v[208:211], v159 offset:16384
	ds_read_b128 v[212:215], v159 offset:17408
	s_add_i32 s0, s23, 2
	s_ashr_i32 s1, s0, 31
	s_add_i32 s22, s22, 2
	s_lshl_b64 s[0:1], s[0:1], 7
	s_add_u32 s24, s20, s0
	s_addc_u32 s25, s21, s1
	v_readfirstlane_b32 s26, v152
	v_lshl_add_u64 v[232:233], s[24:25], 0, v[138:139]
	s_mov_b32 m0, s26
	s_nop 0
	global_load_lds_dwordx4 v[232:233], off
	v_lshl_add_u64 v[232:233], s[24:25], 0, v[140:141]
	v_readfirstlane_b32 s24, v133
	s_mov_b32 m0, s24
	s_nop 0
	global_load_lds_dwordx4 v[232:233], off
	s_add_u32 s24, s12, s0
	s_addc_u32 s25, s13, s1
	v_readfirstlane_b32 s26, v1
	v_lshl_add_u64 v[232:233], s[24:25], 0, v[142:143]
	s_mov_b32 m0, s26
	s_nop 0
	global_load_lds_dwordx4 v[232:233], off
	v_lshl_add_u64 v[232:233], s[24:25], 0, v[144:145]
	v_readfirstlane_b32 s24, v146
	s_mov_b32 m0, s24
	s_nop 0
	global_load_lds_dwordx4 v[232:233], off
	s_add_u32 s24, s14, s0
	s_addc_u32 s25, s15, s1
	v_readfirstlane_b32 s26, v153
	v_lshl_add_u64 v[232:233], s[24:25], 0, v[138:139]
	s_mov_b32 m0, s26
	s_nop 0
	global_load_lds_dwordx4 v[232:233], off
	v_lshl_add_u64 v[232:233], s[24:25], 0, v[140:141]
	v_readfirstlane_b32 s24, v147
	s_mov_b32 m0, s24
	s_nop 0
	global_load_lds_dwordx4 v[232:233], off
	s_waitcnt vmcnt(6)
	s_waitcnt lgkmcnt(0)
	s_barrier
	s_setprio 1
	v_mfma_f32_16x16x32_f16 v[66:69], v[168:171], v[184:187], v[66:69]
	v_mfma_f32_16x16x32_f16 v[62:65], v[176:179], v[184:187], v[62:65]
	v_mfma_f32_16x16x32_f16 v[58:61], v[168:171], v[192:195], v[58:61]
	v_mfma_f32_16x16x32_f16 v[54:57], v[176:179], v[192:195], v[54:57]
	v_mfma_f32_16x16x32_f16 v[50:53], v[168:171], v[200:203], v[50:53]
	v_mfma_f32_16x16x32_f16 v[46:49], v[176:179], v[200:203], v[46:49]
	v_mfma_f32_16x16x32_f16 v[42:45], v[168:171], v[208:211], v[42:45]
	v_mfma_f32_16x16x32_f16 v[38:41], v[176:179], v[208:211], v[38:41]
	v_mfma_f32_16x16x32_f16 v[66:69], v[172:175], v[188:191], v[66:69]
	v_mfma_f32_16x16x32_f16 v[62:65], v[180:183], v[188:191], v[62:65]
	v_mfma_f32_16x16x32_f16 v[58:61], v[172:175], v[196:199], v[58:61]
	v_mfma_f32_16x16x32_f16 v[54:57], v[180:183], v[196:199], v[54:57]
	v_mfma_f32_16x16x32_f16 v[50:53], v[172:175], v[204:207], v[50:53]
	v_mfma_f32_16x16x32_f16 v[46:49], v[180:183], v[204:207], v[46:49]
	v_mfma_f32_16x16x32_f16 v[42:45], v[172:175], v[212:215], v[42:45]
	v_mfma_f32_16x16x32_f16 v[38:41], v[180:183], v[212:215], v[38:41]
	v_mfma_f32_16x16x32_f16 v[34:37], v[216:219], v[184:187], v[34:37]
	v_mfma_f32_16x16x32_f16 v[30:33], v[224:227], v[184:187], v[30:33]
	v_mfma_f32_16x16x32_f16 v[26:29], v[216:219], v[192:195], v[26:29]
	v_mfma_f32_16x16x32_f16 v[22:25], v[224:227], v[192:195], v[22:25]
	v_mfma_f32_16x16x32_f16 v[18:21], v[216:219], v[200:203], v[18:21]
	v_mfma_f32_16x16x32_f16 v[14:17], v[224:227], v[200:203], v[14:17]
	v_mfma_f32_16x16x32_f16 v[10:13], v[216:219], v[208:211], v[10:13]
	v_mfma_f32_16x16x32_f16 v[6:9], v[224:227], v[208:211], v[6:9]
	v_mfma_f32_16x16x32_f16 v[34:37], v[220:223], v[188:191], v[34:37]
	v_mfma_f32_16x16x32_f16 v[30:33], v[228:231], v[188:191], v[30:33]
	v_mfma_f32_16x16x32_f16 v[26:29], v[220:223], v[196:199], v[26:29]
	v_mfma_f32_16x16x32_f16 v[22:25], v[228:231], v[196:199], v[22:25]
	v_mfma_f32_16x16x32_f16 v[18:21], v[220:223], v[204:207], v[18:21]
	v_mfma_f32_16x16x32_f16 v[14:17], v[228:231], v[204:207], v[14:17]
	v_mfma_f32_16x16x32_f16 v[10:13], v[220:223], v[212:215], v[10:13]
	v_mfma_f32_16x16x32_f16 v[6:9], v[228:231], v[212:215], v[6:9]
	s_setprio 0
	s_barrier
	ds_read_b128 v[168:171], v149
	ds_read_b128 v[172:175], v149 offset:1024
	ds_read_b128 v[176:179], v149 offset:2048
	ds_read_b128 v[180:183], v149 offset:3072
	s_add_u32 s0, s2, s0
	s_addc_u32 s1, s3, s1
	v_readfirstlane_b32 s24, v162
	v_lshl_add_u64 v[216:217], s[0:1], 0, v[142:143]
	s_mov_b32 m0, s24
	ds_read_b128 v[184:187], v156 offset:32768
	ds_read_b128 v[188:191], v156 offset:33792
	ds_read_b128 v[192:195], v157 offset:32768
	ds_read_b128 v[196:199], v157 offset:33792
	ds_read_b128 v[200:203], v158 offset:32768
	ds_read_b128 v[204:207], v158 offset:33792
	ds_read_b128 v[208:211], v159 offset:32768
	ds_read_b128 v[212:215], v159 offset:33792
	global_load_lds_dwordx4 v[216:217], off
	v_lshl_add_u64 v[216:217], s[0:1], 0, v[144:145]
	v_readfirstlane_b32 s0, v163
	s_mov_b32 m0, s0
	s_nop 0
	global_load_lds_dwordx4 v[216:217], off
	ds_read_b128 v[216:219], v148
	ds_read_b128 v[220:223], v148 offset:1024
	ds_read_b128 v[224:227], v148 offset:2048
	ds_read_b128 v[228:231], v148 offset:3072
	s_waitcnt lgkmcnt(0)
	s_barrier
	s_setprio 1
	v_mfma_f32_16x16x32_f16 v[2:5], v[168:171], v[184:187], v[2:5]
	v_mfma_f32_16x16x32_f16 v[126:129], v[176:179], v[184:187], v[126:129]
	v_mfma_f32_16x16x32_f16 v[122:125], v[168:171], v[192:195], v[122:125]
	v_mfma_f32_16x16x32_f16 v[118:121], v[176:179], v[192:195], v[118:121]
	v_mfma_f32_16x16x32_f16 v[114:117], v[168:171], v[200:203], v[114:117]
	v_mfma_f32_16x16x32_f16 v[110:113], v[176:179], v[200:203], v[110:113]
	v_mfma_f32_16x16x32_f16 v[106:109], v[168:171], v[208:211], v[106:109]
	v_mfma_f32_16x16x32_f16 v[102:105], v[176:179], v[208:211], v[102:105]
	v_mfma_f32_16x16x32_f16 v[2:5], v[172:175], v[188:191], v[2:5]
	v_mfma_f32_16x16x32_f16 v[126:129], v[180:183], v[188:191], v[126:129]
	v_mfma_f32_16x16x32_f16 v[122:125], v[172:175], v[196:199], v[122:125]
	v_mfma_f32_16x16x32_f16 v[118:121], v[180:183], v[196:199], v[118:121]
	v_mfma_f32_16x16x32_f16 v[114:117], v[172:175], v[204:207], v[114:117]
	v_mfma_f32_16x16x32_f16 v[110:113], v[180:183], v[204:207], v[110:113]
	v_mfma_f32_16x16x32_f16 v[106:109], v[172:175], v[212:215], v[106:109]
	v_mfma_f32_16x16x32_f16 v[102:105], v[180:183], v[212:215], v[102:105]
	v_mfma_f32_16x16x32_f16 v[98:101], v[216:219], v[184:187], v[98:101]
	v_mfma_f32_16x16x32_f16 v[94:97], v[224:227], v[184:187], v[94:97]
	v_mfma_f32_16x16x32_f16 v[90:93], v[216:219], v[192:195], v[90:93]
	v_mfma_f32_16x16x32_f16 v[86:89], v[224:227], v[192:195], v[86:89]
	v_mfma_f32_16x16x32_f16 v[82:85], v[216:219], v[200:203], v[82:85]
	v_mfma_f32_16x16x32_f16 v[78:81], v[224:227], v[200:203], v[78:81]
	v_mfma_f32_16x16x32_f16 v[74:77], v[216:219], v[208:211], v[74:77]
	v_mfma_f32_16x16x32_f16 v[70:73], v[224:227], v[208:211], v[70:73]
	v_mfma_f32_16x16x32_f16 v[98:101], v[220:223], v[188:191], v[98:101]
	v_mfma_f32_16x16x32_f16 v[94:97], v[228:231], v[188:191], v[94:97]
	v_mfma_f32_16x16x32_f16 v[90:93], v[220:223], v[196:199], v[90:93]
	v_mfma_f32_16x16x32_f16 v[86:89], v[228:231], v[196:199], v[86:89]
	v_mfma_f32_16x16x32_f16 v[82:85], v[220:223], v[204:207], v[82:85]
	v_mfma_f32_16x16x32_f16 v[78:81], v[228:231], v[204:207], v[78:81]
	v_mfma_f32_16x16x32_f16 v[74:77], v[220:223], v[212:215], v[74:77]
	v_mfma_f32_16x16x32_f16 v[70:73], v[228:231], v[212:215], v[70:73]
	s_setprio 0
	s_barrier
	ds_read_b128 v[184:187], v156 offset:49152
	ds_read_b128 v[188:191], v156 offset:50176
	ds_read_b128 v[192:195], v157 offset:49152
	ds_read_b128 v[196:199], v157 offset:50176
	ds_read_b128 v[200:203], v158 offset:49152
	ds_read_b128 v[204:207], v158 offset:50176
	ds_read_b128 v[208:211], v159 offset:49152
	ds_read_b128 v[212:215], v159 offset:50176
	s_add_i32 s0, s23, 3
	s_ashr_i32 s1, s0, 31
	s_lshl_b64 s[0:1], s[0:1], 7
	s_add_u32 s24, s20, s0
	s_addc_u32 s25, s21, s1
	v_readfirstlane_b32 s23, v154
	v_lshl_add_u64 v[232:233], s[24:25], 0, v[138:139]
	s_mov_b32 m0, s23
	v_readfirstlane_b32 s23, v164
	global_load_lds_dwordx4 v[232:233], off
	v_lshl_add_u64 v[232:233], s[24:25], 0, v[140:141]
	s_mov_b32 m0, s23
	s_nop 0
	global_load_lds_dwordx4 v[232:233], off
	s_add_u32 s24, s12, s0
	s_addc_u32 s25, s13, s1
	v_readfirstlane_b32 s23, v165
	v_lshl_add_u64 v[232:233], s[24:25], 0, v[142:143]
	s_mov_b32 m0, s23
	v_readfirstlane_b32 s23, v166
	global_load_lds_dwordx4 v[232:233], off
	v_lshl_add_u64 v[232:233], s[24:25], 0, v[144:145]
	s_mov_b32 m0, s23
	s_nop 0
	global_load_lds_dwordx4 v[232:233], off
	s_add_u32 s0, s14, s0
	s_addc_u32 s1, s15, s1
	v_readfirstlane_b32 s23, v155
	v_lshl_add_u64 v[232:233], s[0:1], 0, v[138:139]
	s_mov_b32 m0, s23
	s_nop 0
	global_load_lds_dwordx4 v[232:233], off
	v_lshl_add_u64 v[232:233], s[0:1], 0, v[140:141]
	v_readfirstlane_b32 s0, v167
	s_mov_b32 m0, s0
	s_nop 0
	global_load_lds_dwordx4 v[232:233], off
	s_waitcnt vmcnt(6)
	s_waitcnt lgkmcnt(0)
	s_barrier
	s_setprio 1
	v_mfma_f32_16x16x32_f16 v[66:69], v[168:171], v[184:187], v[66:69]
	v_mfma_f32_16x16x32_f16 v[62:65], v[176:179], v[184:187], v[62:65]
	v_mfma_f32_16x16x32_f16 v[58:61], v[168:171], v[192:195], v[58:61]
	v_mfma_f32_16x16x32_f16 v[54:57], v[176:179], v[192:195], v[54:57]
	v_mfma_f32_16x16x32_f16 v[50:53], v[168:171], v[200:203], v[50:53]
	v_mfma_f32_16x16x32_f16 v[46:49], v[176:179], v[200:203], v[46:49]
	v_mfma_f32_16x16x32_f16 v[42:45], v[168:171], v[208:211], v[42:45]
	v_mfma_f32_16x16x32_f16 v[38:41], v[176:179], v[208:211], v[38:41]
	v_mfma_f32_16x16x32_f16 v[66:69], v[172:175], v[188:191], v[66:69]
	v_mfma_f32_16x16x32_f16 v[62:65], v[180:183], v[188:191], v[62:65]
	v_mfma_f32_16x16x32_f16 v[58:61], v[172:175], v[196:199], v[58:61]
	v_mfma_f32_16x16x32_f16 v[54:57], v[180:183], v[196:199], v[54:57]
	v_mfma_f32_16x16x32_f16 v[50:53], v[172:175], v[204:207], v[50:53]
	v_mfma_f32_16x16x32_f16 v[46:49], v[180:183], v[204:207], v[46:49]
	v_mfma_f32_16x16x32_f16 v[42:45], v[172:175], v[212:215], v[42:45]
	v_mfma_f32_16x16x32_f16 v[38:41], v[180:183], v[212:215], v[38:41]
	v_mfma_f32_16x16x32_f16 v[34:37], v[216:219], v[184:187], v[34:37]
	v_mfma_f32_16x16x32_f16 v[30:33], v[224:227], v[184:187], v[30:33]
	v_mfma_f32_16x16x32_f16 v[26:29], v[216:219], v[192:195], v[26:29]
	v_mfma_f32_16x16x32_f16 v[22:25], v[224:227], v[192:195], v[22:25]
	v_mfma_f32_16x16x32_f16 v[18:21], v[216:219], v[200:203], v[18:21]
	v_mfma_f32_16x16x32_f16 v[14:17], v[224:227], v[200:203], v[14:17]
	v_mfma_f32_16x16x32_f16 v[10:13], v[216:219], v[208:211], v[10:13]
	v_mfma_f32_16x16x32_f16 v[6:9], v[224:227], v[208:211], v[6:9]
	v_mfma_f32_16x16x32_f16 v[34:37], v[220:223], v[188:191], v[34:37]
	v_mfma_f32_16x16x32_f16 v[30:33], v[228:231], v[188:191], v[30:33]
	v_mfma_f32_16x16x32_f16 v[26:29], v[220:223], v[196:199], v[26:29]
	v_mfma_f32_16x16x32_f16 v[22:25], v[228:231], v[196:199], v[22:25]
	v_mfma_f32_16x16x32_f16 v[18:21], v[220:223], v[204:207], v[18:21]
	v_mfma_f32_16x16x32_f16 v[14:17], v[228:231], v[204:207], v[14:17]
	v_mfma_f32_16x16x32_f16 v[10:13], v[220:223], v[212:215], v[10:13]
	v_mfma_f32_16x16x32_f16 v[6:9], v[228:231], v[212:215], v[6:9]
	s_setprio 0
	s_cmp_lt_i32 s22, s36
	s_barrier
	s_cbranch_scc1 .LBB4_203

.LBB7_2:
	s_or_b64 exec, exec, s[8:9]
	s_add_i32 s20, s14, 1
	s_ashr_i32 s21, s20, 31
	s_lshl_b64 s[8:9], s[20:21], 7
	s_add_u32 s16, s3, s8
	s_addc_u32 s17, s37, s9
	s_add_i32 s22, 0, 0x18000
	v_add_u32_e32 v164, s22, v2
	v_lshl_add_u64 v[4:5], s[16:17], 0, v[142:143]
	v_readfirstlane_b32 s23, v164
	s_mov_b32 m0, s23
	v_add_u32_e32 v6, 0x2000, v164
	s_waitcnt vmcnt(2)
	s_barrier
	global_load_lds_dwordx4 v[4:5], off
	v_lshl_add_u64 v[4:5], s[16:17], 0, v[144:145]
	v_readfirstlane_b32 s16, v6
	s_mov_b32 m0, s16
	s_add_u32 s16, s38, s8
	s_addc_u32 s17, s39, s9
	v_add_u32_e32 v6, 0x8000, v1
	s_add_u32 s8, s40, s8
	v_readfirstlane_b32 s23, v6
	global_load_lds_dwordx4 v[4:5], off
	v_lshl_add_u64 v[4:5], v[138:139], 1, s[16:17]
	s_mov_b32 m0, s23
	v_add_u32_e32 v6, 0xa000, v1
	s_addc_u32 s9, s41, s9
	s_add_i32 s23, 0, 0x1c000
	global_load_lds_dwordx4 v[4:5], off
	v_lshl_add_u64 v[4:5], v[140:141], 1, s[16:17]
	v_readfirstlane_b32 s16, v6
	v_add_u32_e32 v165, s23, v2
	s_mov_b32 m0, s16
	v_readfirstlane_b32 s16, v165
	global_load_lds_dwordx4 v[4:5], off
	v_lshl_add_u64 v[4:5], s[8:9], 0, v[142:143]
	s_mov_b32 m0, s16
	v_add_u32_e32 v2, 0x2000, v165
	global_load_lds_dwordx4 v[4:5], off
	v_lshl_add_u64 v[4:5], s[8:9], 0, v[144:145]
	v_readfirstlane_b32 s8, v2
	s_mov_b32 m0, s8
	s_cmp_gt_i32 s11, 2
	global_load_lds_dwordx4 v[4:5], off
	v_lshlrev_b32_e32 v4, 6, v0
	v_lshlrev_b32_e32 v5, 2, v0
	s_waitcnt vmcnt(6)
	v_and_b32_e32 v155, 48, v0
	v_and_b32_e32 v4, 0x3c0, v4
	v_and_b32_e32 v5, 32, v5
	v_bfe_u32 v152, v0, 6, 2
	s_cselect_b64 s[16:17], -1, 0
	v_bitop3_b32 v4, v4, v5, v155 bitop3:0x36
	v_lshlrev_b32_e32 v135, 6, v3
	v_and_b32_e32 v131, 15, v0
	v_lshlrev_b32_e32 v2, 12, v152
	v_add_u32_e32 v5, s12, v4
	v_add_u32_e32 v6, s13, v4
	v_add_u32_e32 v7, s22, v4
	v_add_u32_e32 v8, s23, v4
	s_and_b64 vcc, exec, s[16:17]
	v_lshlrev_b32_e32 v153, 13, v3
	v_or_b32_e32 v166, 16, v135
	v_or_b32_e32 v157, 32, v135
	v_or_b32_e32 v156, 48, v135
	s_barrier
	s_cbranch_vccnz .LBB7_4
	v_lshlrev_b32_e32 v154, 13, v3
	v_or_b32_e32 v3, v166, v131
	v_lshlrev_b32_e32 v9, 6, v3
	v_lshlrev_b32_e32 v3, 2, v3
	v_and_b32_e32 v9, 0x3c0, v9
	v_and_b32_e32 v3, 32, v3
	v_bitop3_b32 v130, v9, v3, v155 bitop3:0x36
	v_or_b32_e32 v3, v157, v131
	v_lshlrev_b32_e32 v9, 6, v3
	v_lshlrev_b32_e32 v3, 2, v3
	v_and_b32_e32 v9, 0x3c0, v9
	v_and_b32_e32 v3, 32, v3
	v_bitop3_b32 v134, v9, v3, v155 bitop3:0x36
	v_or_b32_e32 v3, v156, v131
	v_lshlrev_b32_e32 v9, 6, v3
	v_lshlrev_b32_e32 v3, 2, v3
	v_and_b32_e32 v9, 0x3c0, v9
	v_and_b32_e32 v3, 32, v3
	v_lshlrev_b32_e32 v132, 7, v166
	v_lshlrev_b32_e32 v136, 7, v157
	v_bitop3_b32 v137, v9, v3, v155 bitop3:0x36
	v_lshlrev_b32_e32 v150, 7, v156
	s_mov_b64 s[22:23], 0
	s_branch .LBB7_5

.LBB7_7:
	ds_read_b128 v[178:181], v161
	ds_read_b128 v[182:185], v161 offset:1024
	ds_read_b128 v[186:189], v161 offset:2048
	ds_read_b128 v[190:193], v161 offset:3072
	s_add_i32 s23, s14, s22
	s_add_i32 s0, s23, 1
	s_ashr_i32 s1, s0, 31
	s_lshl_b64 s[0:1], s[0:1], 7
	s_add_u32 s0, s42, s0
	s_addc_u32 s1, s43, s1
	v_readfirstlane_b32 s44, v166
	v_lshl_add_u64 v[194:195], s[0:1], 0, v[146:147]
	s_mov_b32 m0, s44
	s_nop 0
	global_load_lds_dwordx4 v[194:195], off
	v_lshl_add_u64 v[194:195], s[0:1], 0, v[148:149]
	v_readfirstlane_b32 s0, v167
	s_mov_b32 m0, s0
	s_nop 0
	global_load_lds_dwordx4 v[194:195], off
	ds_read_b128 v[194:197], v154
	ds_read_b128 v[198:201], v154 offset:1024
	ds_read_b128 v[202:205], v155
	ds_read_b128 v[206:209], v155 offset:1024
	ds_read_b128 v[210:213], v156
	ds_read_b128 v[214:217], v156 offset:1024
	ds_read_b128 v[218:221], v157
	ds_read_b128 v[222:225], v157 offset:1024
	ds_read_b128 v[226:229], v160
	ds_read_b128 v[230:233], v160 offset:1024
	ds_read_b128 v[234:237], v160 offset:2048
	ds_read_b128 v[238:241], v160 offset:3072
	s_waitcnt lgkmcnt(0)
	s_barrier
	s_setprio 1
	v_mfma_f32_16x16x32_f16 v[110:113], v[178:181], v[194:197], v[110:113]
	v_mfma_f32_16x16x32_f16 v[126:129], v[186:189], v[194:197], v[126:129]
	v_mfma_f32_16x16x32_f16 v[122:125], v[178:181], v[202:205], v[122:125]
	v_mfma_f32_16x16x32_f16 v[118:121], v[186:189], v[202:205], v[118:121]
	v_mfma_f32_16x16x32_f16 v[114:117], v[178:181], v[210:213], v[114:117]
	v_mfma_f32_16x16x32_f16 v[106:109], v[186:189], v[210:213], v[106:109]
	v_mfma_f32_16x16x32_f16 v[102:105], v[178:181], v[218:221], v[102:105]
	v_mfma_f32_16x16x32_f16 v[98:101], v[186:189], v[218:221], v[98:101]
	v_mfma_f32_16x16x32_f16 v[110:113], v[182:185], v[198:201], v[110:113]
	v_mfma_f32_16x16x32_f16 v[126:129], v[190:193], v[198:201], v[126:129]
	v_mfma_f32_16x16x32_f16 v[122:125], v[182:185], v[206:209], v[122:125]
	v_mfma_f32_16x16x32_f16 v[118:121], v[190:193], v[206:209], v[118:121]
	v_mfma_f32_16x16x32_f16 v[114:117], v[182:185], v[214:217], v[114:117]
	v_mfma_f32_16x16x32_f16 v[106:109], v[190:193], v[214:217], v[106:109]
	v_mfma_f32_16x16x32_f16 v[102:105], v[182:185], v[222:225], v[102:105]
	v_mfma_f32_16x16x32_f16 v[98:101], v[190:193], v[222:225], v[98:101]
	v_mfma_f32_16x16x32_f16 v[94:97], v[226:229], v[194:197], v[94:97]
	v_mfma_f32_16x16x32_f16 v[90:93], v[234:237], v[194:197], v[90:93]
	v_mfma_f32_16x16x32_f16 v[86:89], v[226:229], v[202:205], v[86:89]
	v_mfma_f32_16x16x32_f16 v[82:85], v[234:237], v[202:205], v[82:85]
	v_mfma_f32_16x16x32_f16 v[78:81], v[226:229], v[210:213], v[78:81]
	v_mfma_f32_16x16x32_f16 v[74:77], v[234:237], v[210:213], v[74:77]
	v_mfma_f32_16x16x32_f16 v[70:73], v[226:229], v[218:221], v[70:73]
	v_mfma_f32_16x16x32_f16 v[66:69], v[234:237], v[218:221], v[66:69]
	v_mfma_f32_16x16x32_f16 v[94:97], v[230:233], v[198:201], v[94:97]
	v_mfma_f32_16x16x32_f16 v[90:93], v[238:241], v[198:201], v[90:93]
	v_mfma_f32_16x16x32_f16 v[86:89], v[230:233], v[206:209], v[86:89]
	v_mfma_f32_16x16x32_f16 v[82:85], v[238:241], v[206:209], v[82:85]
	v_mfma_f32_16x16x32_f16 v[78:81], v[230:233], v[214:217], v[78:81]
	v_mfma_f32_16x16x32_f16 v[74:77], v[238:241], v[214:217], v[74:77]
	v_mfma_f32_16x16x32_f16 v[70:73], v[230:233], v[222:225], v[70:73]
	v_mfma_f32_16x16x32_f16 v[66:69], v[238:241], v[222:225], v[66:69]
	s_setprio 0
	s_barrier
	ds_read_b128 v[194:197], v154 offset:16384
	ds_read_b128 v[198:201], v154 offset:17408
	ds_read_b128 v[202:205], v155 offset:16384
	ds_read_b128 v[206:209], v155 offset:17408
	ds_read_b128 v[210:213], v156 offset:16384
	ds_read_b128 v[214:217], v156 offset:17408
	ds_read_b128 v[218:221], v157 offset:16384
	ds_read_b128 v[222:225], v157 offset:17408
	s_add_i32 s0, s23, 2
	s_ashr_i32 s1, s0, 31
	s_add_i32 s22, s22, 2
	s_lshl_b64 s[0:1], s[0:1], 7
	s_add_u32 s44, s3, s0
	s_addc_u32 s45, s37, s1
	v_readfirstlane_b32 s46, v162
	v_lshl_add_u64 v[242:243], s[44:45], 0, v[142:143]
	s_mov_b32 m0, s46
	s_nop 0
	global_load_lds_dwordx4 v[242:243], off
	v_lshl_add_u64 v[242:243], s[44:45], 0, v[144:145]
	v_readfirstlane_b32 s44, v168
	s_mov_b32 m0, s44
	s_nop 0
	global_load_lds_dwordx4 v[242:243], off
	s_add_u32 s44, s38, s0
	s_addc_u32 s45, s39, s1
	v_readfirstlane_b32 s46, v1
	v_lshl_add_u64 v[242:243], s[44:45], 0, v[146:147]
	s_mov_b32 m0, s46
	s_nop 0
	global_load_lds_dwordx4 v[242:243], off
	v_lshl_add_u64 v[242:243], s[44:45], 0, v[148:149]
	v_readfirstlane_b32 s44, v169
	s_mov_b32 m0, s44
	s_nop 0
	global_load_lds_dwordx4 v[242:243], off
	s_add_u32 s44, s40, s0
	s_addc_u32 s45, s41, s1
	v_readfirstlane_b32 s46, v163
	v_lshl_add_u64 v[242:243], s[44:45], 0, v[142:143]
	s_mov_b32 m0, s46
	s_nop 0
	global_load_lds_dwordx4 v[242:243], off
	v_lshl_add_u64 v[242:243], s[44:45], 0, v[144:145]
	v_readfirstlane_b32 s44, v170
	s_mov_b32 m0, s44
	s_nop 0
	global_load_lds_dwordx4 v[242:243], off
	s_waitcnt vmcnt(6)
	s_waitcnt lgkmcnt(0)
	s_barrier
	s_setprio 1
	v_mfma_f32_16x16x32_f16 v[62:65], v[178:181], v[194:197], v[62:65]
	v_mfma_f32_16x16x32_f16 v[58:61], v[186:189], v[194:197], v[58:61]
	v_mfma_f32_16x16x32_f16 v[54:57], v[178:181], v[202:205], v[54:57]
	v_mfma_f32_16x16x32_f16 v[50:53], v[186:189], v[202:205], v[50:53]
	v_mfma_f32_16x16x32_f16 v[46:49], v[178:181], v[210:213], v[46:49]
	v_mfma_f32_16x16x32_f16 v[42:45], v[186:189], v[210:213], v[42:45]
	v_mfma_f32_16x16x32_f16 v[38:41], v[178:181], v[218:221], v[38:41]
	v_mfma_f32_16x16x32_f16 v[34:37], v[186:189], v[218:221], v[34:37]
	v_mfma_f32_16x16x32_f16 v[62:65], v[182:185], v[198:201], v[62:65]
	v_mfma_f32_16x16x32_f16 v[58:61], v[190:193], v[198:201], v[58:61]
	v_mfma_f32_16x16x32_f16 v[54:57], v[182:185], v[206:209], v[54:57]
	v_mfma_f32_16x16x32_f16 v[50:53], v[190:193], v[206:209], v[50:53]
	v_mfma_f32_16x16x32_f16 v[46:49], v[182:185], v[214:217], v[46:49]
	v_mfma_f32_16x16x32_f16 v[42:45], v[190:193], v[214:217], v[42:45]
	v_mfma_f32_16x16x32_f16 v[38:41], v[182:185], v[222:225], v[38:41]
	v_mfma_f32_16x16x32_f16 v[34:37], v[190:193], v[222:225], v[34:37]
	v_mfma_f32_16x16x32_f16 v[30:33], v[226:229], v[194:197], v[30:33]
	v_mfma_f32_16x16x32_f16 v[26:29], v[234:237], v[194:197], v[26:29]
	v_mfma_f32_16x16x32_f16 v[22:25], v[226:229], v[202:205], v[22:25]
	v_mfma_f32_16x16x32_f16 v[18:21], v[234:237], v[202:205], v[18:21]
	v_mfma_f32_16x16x32_f16 v[14:17], v[226:229], v[210:213], v[14:17]
	v_mfma_f32_16x16x32_f16 v[10:13], v[234:237], v[210:213], v[10:13]
	v_mfma_f32_16x16x32_f16 v[6:9], v[226:229], v[218:221], v[6:9]
	v_mfma_f32_16x16x32_f16 v[2:5], v[234:237], v[218:221], v[2:5]
	v_mfma_f32_16x16x32_f16 v[30:33], v[230:233], v[198:201], v[30:33]
	v_mfma_f32_16x16x32_f16 v[26:29], v[238:241], v[198:201], v[26:29]
	v_mfma_f32_16x16x32_f16 v[22:25], v[230:233], v[206:209], v[22:25]
	v_mfma_f32_16x16x32_f16 v[18:21], v[238:241], v[206:209], v[18:21]
	v_mfma_f32_16x16x32_f16 v[14:17], v[230:233], v[214:217], v[14:17]
	v_mfma_f32_16x16x32_f16 v[10:13], v[238:241], v[214:217], v[10:13]
	v_mfma_f32_16x16x32_f16 v[6:9], v[230:233], v[222:225], v[6:9]
	v_mfma_f32_16x16x32_f16 v[2:5], v[238:241], v[222:225], v[2:5]
	s_setprio 0
	s_barrier
	ds_read_b128 v[178:181], v159
	ds_read_b128 v[182:185], v159 offset:1024
	ds_read_b128 v[186:189], v159 offset:2048
	ds_read_b128 v[190:193], v159 offset:3072
	s_add_u32 s0, s42, s0
	s_addc_u32 s1, s43, s1
	v_readfirstlane_b32 s44, v171
	v_lshl_add_u64 v[226:227], s[0:1], 0, v[146:147]
	s_mov_b32 m0, s44
	ds_read_b128 v[194:197], v154 offset:32768
	ds_read_b128 v[198:201], v154 offset:33792
	ds_read_b128 v[202:205], v155 offset:32768
	ds_read_b128 v[206:209], v155 offset:33792
	ds_read_b128 v[210:213], v156 offset:32768
	ds_read_b128 v[214:217], v156 offset:33792
	ds_read_b128 v[218:221], v157 offset:32768
	ds_read_b128 v[222:225], v157 offset:33792
	global_load_lds_dwordx4 v[226:227], off
	v_lshl_add_u64 v[226:227], s[0:1], 0, v[148:149]
	v_readfirstlane_b32 s0, v172
	s_mov_b32 m0, s0
	s_nop 0
	global_load_lds_dwordx4 v[226:227], off
	ds_read_b128 v[226:229], v158
	ds_read_b128 v[230:233], v158 offset:1024
	ds_read_b128 v[234:237], v158 offset:2048
	ds_read_b128 v[238:241], v158 offset:3072
	s_waitcnt lgkmcnt(0)
	s_barrier
	s_setprio 1
	v_mfma_f32_16x16x32_f16 v[110:113], v[178:181], v[194:197], v[110:113]
	v_mfma_f32_16x16x32_f16 v[126:129], v[186:189], v[194:197], v[126:129]
	v_mfma_f32_16x16x32_f16 v[122:125], v[178:181], v[202:205], v[122:125]
	v_mfma_f32_16x16x32_f16 v[118:121], v[186:189], v[202:205], v[118:121]
	v_mfma_f32_16x16x32_f16 v[114:117], v[178:181], v[210:213], v[114:117]
	v_mfma_f32_16x16x32_f16 v[106:109], v[186:189], v[210:213], v[106:109]
	v_mfma_f32_16x16x32_f16 v[102:105], v[178:181], v[218:221], v[102:105]
	v_mfma_f32_16x16x32_f16 v[98:101], v[186:189], v[218:221], v[98:101]
	v_mfma_f32_16x16x32_f16 v[110:113], v[182:185], v[198:201], v[110:113]
	v_mfma_f32_16x16x32_f16 v[126:129], v[190:193], v[198:201], v[126:129]
	v_mfma_f32_16x16x32_f16 v[122:125], v[182:185], v[206:209], v[122:125]
	v_mfma_f32_16x16x32_f16 v[118:121], v[190:193], v[206:209], v[118:121]
	v_mfma_f32_16x16x32_f16 v[114:117], v[182:185], v[214:217], v[114:117]
	v_mfma_f32_16x16x32_f16 v[106:109], v[190:193], v[214:217], v[106:109]
	v_mfma_f32_16x16x32_f16 v[102:105], v[182:185], v[222:225], v[102:105]
	v_mfma_f32_16x16x32_f16 v[98:101], v[190:193], v[222:225], v[98:101]
	v_mfma_f32_16x16x32_f16 v[94:97], v[226:229], v[194:197], v[94:97]
	v_mfma_f32_16x16x32_f16 v[90:93], v[234:237], v[194:197], v[90:93]
	v_mfma_f32_16x16x32_f16 v[86:89], v[226:229], v[202:205], v[86:89]
	v_mfma_f32_16x16x32_f16 v[82:85], v[234:237], v[202:205], v[82:85]
	v_mfma_f32_16x16x32_f16 v[78:81], v[226:229], v[210:213], v[78:81]
	v_mfma_f32_16x16x32_f16 v[74:77], v[234:237], v[210:213], v[74:77]
	v_mfma_f32_16x16x32_f16 v[70:73], v[226:229], v[218:221], v[70:73]
	v_mfma_f32_16x16x32_f16 v[66:69], v[234:237], v[218:221], v[66:69]
	v_mfma_f32_16x16x32_f16 v[94:97], v[230:233], v[198:201], v[94:97]
	v_mfma_f32_16x16x32_f16 v[90:93], v[238:241], v[198:201], v[90:93]
	v_mfma_f32_16x16x32_f16 v[86:89], v[230:233], v[206:209], v[86:89]
	v_mfma_f32_16x16x32_f16 v[82:85], v[238:241], v[206:209], v[82:85]
	v_mfma_f32_16x16x32_f16 v[78:81], v[230:233], v[214:217], v[78:81]
	v_mfma_f32_16x16x32_f16 v[74:77], v[238:241], v[214:217], v[74:77]
	v_mfma_f32_16x16x32_f16 v[70:73], v[230:233], v[222:225], v[70:73]
	v_mfma_f32_16x16x32_f16 v[66:69], v[238:241], v[222:225], v[66:69]
	s_setprio 0
	s_barrier
	ds_read_b128 v[194:197], v154 offset:49152
	ds_read_b128 v[198:201], v154 offset:50176
	ds_read_b128 v[202:205], v155 offset:49152
	ds_read_b128 v[206:209], v155 offset:50176
	ds_read_b128 v[210:213], v156 offset:49152
	ds_read_b128 v[214:217], v156 offset:50176
	ds_read_b128 v[218:221], v157 offset:49152
	ds_read_b128 v[222:225], v157 offset:50176
	s_add_i32 s0, s23, 3
	s_ashr_i32 s1, s0, 31
	s_lshl_b64 s[0:1], s[0:1], 7
	s_add_u32 s44, s3, s0
	s_addc_u32 s45, s37, s1
	v_readfirstlane_b32 s23, v164
	v_lshl_add_u64 v[242:243], s[44:45], 0, v[142:143]
	s_mov_b32 m0, s23
	v_readfirstlane_b32 s23, v173
	global_load_lds_dwordx4 v[242:243], off
	v_lshl_add_u64 v[242:243], s[44:45], 0, v[144:145]
	s_mov_b32 m0, s23
	s_nop 0
	global_load_lds_dwordx4 v[242:243], off
	s_add_u32 s44, s38, s0
	s_addc_u32 s45, s39, s1
	v_readfirstlane_b32 s23, v174
	v_lshl_add_u64 v[242:243], s[44:45], 0, v[146:147]
	s_mov_b32 m0, s23
	v_readfirstlane_b32 s23, v175
	global_load_lds_dwordx4 v[242:243], off
	v_lshl_add_u64 v[242:243], s[44:45], 0, v[148:149]
	s_mov_b32 m0, s23
	s_nop 0
	global_load_lds_dwordx4 v[242:243], off
	s_add_u32 s0, s40, s0
	s_addc_u32 s1, s41, s1
	v_readfirstlane_b32 s23, v165
	v_lshl_add_u64 v[242:243], s[0:1], 0, v[142:143]
	s_mov_b32 m0, s23
	s_nop 0
	global_load_lds_dwordx4 v[242:243], off
	v_lshl_add_u64 v[242:243], s[0:1], 0, v[144:145]
	v_readfirstlane_b32 s0, v176
	s_mov_b32 m0, s0
	s_nop 0
	global_load_lds_dwordx4 v[242:243], off
	s_waitcnt vmcnt(6)
	s_waitcnt lgkmcnt(0)
	s_barrier
	s_setprio 1
	v_mfma_f32_16x16x32_f16 v[62:65], v[178:181], v[194:197], v[62:65]
	v_mfma_f32_16x16x32_f16 v[58:61], v[186:189], v[194:197], v[58:61]
	v_mfma_f32_16x16x32_f16 v[54:57], v[178:181], v[202:205], v[54:57]
	v_mfma_f32_16x16x32_f16 v[50:53], v[186:189], v[202:205], v[50:53]
	v_mfma_f32_16x16x32_f16 v[46:49], v[178:181], v[210:213], v[46:49]
	v_mfma_f32_16x16x32_f16 v[42:45], v[186:189], v[210:213], v[42:45]
	v_mfma_f32_16x16x32_f16 v[38:41], v[178:181], v[218:221], v[38:41]
	v_mfma_f32_16x16x32_f16 v[34:37], v[186:189], v[218:221], v[34:37]
	v_mfma_f32_16x16x32_f16 v[62:65], v[182:185], v[198:201], v[62:65]
	v_mfma_f32_16x16x32_f16 v[58:61], v[190:193], v[198:201], v[58:61]
	v_mfma_f32_16x16x32_f16 v[54:57], v[182:185], v[206:209], v[54:57]
	v_mfma_f32_16x16x32_f16 v[50:53], v[190:193], v[206:209], v[50:53]
	v_mfma_f32_16x16x32_f16 v[46:49], v[182:185], v[214:217], v[46:49]
	v_mfma_f32_16x16x32_f16 v[42:45], v[190:193], v[214:217], v[42:45]
	v_mfma_f32_16x16x32_f16 v[38:41], v[182:185], v[222:225], v[38:41]
	v_mfma_f32_16x16x32_f16 v[34:37], v[190:193], v[222:225], v[34:37]
	v_mfma_f32_16x16x32_f16 v[30:33], v[226:229], v[194:197], v[30:33]
	v_mfma_f32_16x16x32_f16 v[26:29], v[234:237], v[194:197], v[26:29]
	v_mfma_f32_16x16x32_f16 v[22:25], v[226:229], v[202:205], v[22:25]
	v_mfma_f32_16x16x32_f16 v[18:21], v[234:237], v[202:205], v[18:21]
	v_mfma_f32_16x16x32_f16 v[14:17], v[226:229], v[210:213], v[14:17]
	v_mfma_f32_16x16x32_f16 v[10:13], v[234:237], v[210:213], v[10:13]
	v_mfma_f32_16x16x32_f16 v[6:9], v[226:229], v[218:221], v[6:9]
	v_mfma_f32_16x16x32_f16 v[2:5], v[234:237], v[218:221], v[2:5]
	v_mfma_f32_16x16x32_f16 v[30:33], v[230:233], v[198:201], v[30:33]
	v_mfma_f32_16x16x32_f16 v[26:29], v[238:241], v[198:201], v[26:29]
	v_mfma_f32_16x16x32_f16 v[22:25], v[230:233], v[206:209], v[22:25]
	v_mfma_f32_16x16x32_f16 v[18:21], v[238:241], v[206:209], v[18:21]
	v_mfma_f32_16x16x32_f16 v[14:17], v[230:233], v[214:217], v[14:17]
	v_mfma_f32_16x16x32_f16 v[10:13], v[238:241], v[214:217], v[10:13]
	v_mfma_f32_16x16x32_f16 v[6:9], v[230:233], v[222:225], v[6:9]
	v_mfma_f32_16x16x32_f16 v[2:5], v[238:241], v[222:225], v[2:5]
	s_setprio 0
	s_cmp_lt_i32 s22, s24
	s_barrier
	s_cbranch_scc1 .LBB7_7
	v_mov_b32_e32 v154, v153

.LBB7_11:
	ds_read_b128 v[130:133], v161
	ds_read_b128 v[134:137], v161 offset:1024
	ds_read_b128 v[150:153], v161 offset:2048
	ds_read_b128 v[154:157], v161 offset:3072
	s_add_i32 s18, s14, s26
	s_add_i32 s2, s18, 1
	s_ashr_i32 s3, s2, 31
	s_lshl_b64 s[2:3], s[2:3], 7
	s_add_u32 s2, s10, s2
	s_addc_u32 s3, s16, s3
	v_readfirstlane_b32 s19, v173
	v_lshl_add_u64 v[216:217], s[2:3], 0, v[146:147]
	s_mov_b32 m0, s19
	ds_read_b128 v[184:187], v169
	ds_read_b128 v[188:191], v169 offset:1024
	ds_read_b128 v[192:195], v170
	ds_read_b128 v[196:199], v170 offset:1024
	ds_read_b128 v[200:203], v171
	ds_read_b128 v[204:207], v171 offset:1024
	ds_read_b128 v[208:211], v172
	ds_read_b128 v[212:215], v172 offset:1024
	global_load_lds_dwordx4 v[216:217], off
	v_lshl_add_u64 v[216:217], s[2:3], 0, v[148:149]
	v_readfirstlane_b32 s2, v174
	s_mov_b32 m0, s2
	s_nop 0
	global_load_lds_dwordx4 v[216:217], off
	ds_read_b128 v[216:219], v160
	ds_read_b128 v[220:223], v160 offset:1024
	ds_read_b128 v[224:227], v160 offset:2048
	ds_read_b128 v[228:231], v160 offset:3072
	s_waitcnt lgkmcnt(0)
	s_barrier
	s_setprio 1
	v_mfma_f32_16x16x32_f16 v[122:125], v[130:133], v[184:187], v[122:125]
	v_mfma_f32_16x16x32_f16 v[126:129], v[150:153], v[184:187], v[126:129]
	v_mfma_f32_16x16x32_f16 v[118:121], v[130:133], v[192:195], v[118:121]
	v_mfma_f32_16x16x32_f16 v[114:117], v[150:153], v[192:195], v[114:117]
	v_mfma_f32_16x16x32_f16 v[110:113], v[130:133], v[200:203], v[110:113]
	v_mfma_f32_16x16x32_f16 v[106:109], v[150:153], v[200:203], v[106:109]
	v_mfma_f32_16x16x32_f16 v[102:105], v[130:133], v[208:211], v[102:105]
	v_mfma_f32_16x16x32_f16 v[98:101], v[150:153], v[208:211], v[98:101]
	v_mfma_f32_16x16x32_f16 v[122:125], v[134:137], v[188:191], v[122:125]
	v_mfma_f32_16x16x32_f16 v[126:129], v[154:157], v[188:191], v[126:129]
	v_mfma_f32_16x16x32_f16 v[118:121], v[134:137], v[196:199], v[118:121]
	v_mfma_f32_16x16x32_f16 v[114:117], v[154:157], v[196:199], v[114:117]
	v_mfma_f32_16x16x32_f16 v[110:113], v[134:137], v[204:207], v[110:113]
	v_mfma_f32_16x16x32_f16 v[106:109], v[154:157], v[204:207], v[106:109]
	v_mfma_f32_16x16x32_f16 v[102:105], v[134:137], v[212:215], v[102:105]
	v_mfma_f32_16x16x32_f16 v[98:101], v[154:157], v[212:215], v[98:101]
	v_mfma_f32_16x16x32_f16 v[94:97], v[216:219], v[184:187], v[94:97]
	v_mfma_f32_16x16x32_f16 v[90:93], v[224:227], v[184:187], v[90:93]
	v_mfma_f32_16x16x32_f16 v[86:89], v[216:219], v[192:195], v[86:89]
	v_mfma_f32_16x16x32_f16 v[82:85], v[224:227], v[192:195], v[82:85]
	v_mfma_f32_16x16x32_f16 v[78:81], v[216:219], v[200:203], v[78:81]
	v_mfma_f32_16x16x32_f16 v[74:77], v[224:227], v[200:203], v[74:77]
	v_mfma_f32_16x16x32_f16 v[70:73], v[216:219], v[208:211], v[70:73]
	v_mfma_f32_16x16x32_f16 v[66:69], v[224:227], v[208:211], v[66:69]
	v_mfma_f32_16x16x32_f16 v[94:97], v[220:223], v[188:191], v[94:97]
	v_mfma_f32_16x16x32_f16 v[90:93], v[228:231], v[188:191], v[90:93]
	v_mfma_f32_16x16x32_f16 v[86:89], v[220:223], v[196:199], v[86:89]
	v_mfma_f32_16x16x32_f16 v[82:85], v[228:231], v[196:199], v[82:85]
	v_mfma_f32_16x16x32_f16 v[78:81], v[220:223], v[204:207], v[78:81]
	v_mfma_f32_16x16x32_f16 v[74:77], v[228:231], v[204:207], v[74:77]
	v_mfma_f32_16x16x32_f16 v[70:73], v[220:223], v[212:215], v[70:73]
	v_mfma_f32_16x16x32_f16 v[66:69], v[228:231], v[212:215], v[66:69]
	s_setprio 0
	s_barrier
	ds_read_b128 v[184:187], v169 offset:16384
	ds_read_b128 v[188:191], v169 offset:17408
	ds_read_b128 v[192:195], v170 offset:16384
	ds_read_b128 v[196:199], v170 offset:17408
	ds_read_b128 v[200:203], v171 offset:16384
	ds_read_b128 v[204:207], v171 offset:17408
	ds_read_b128 v[208:211], v172 offset:16384
	ds_read_b128 v[212:215], v172 offset:17408
	s_add_i32 s2, s18, 2
	s_ashr_i32 s3, s2, 31
	s_add_i32 s26, s26, 2
	s_lshl_b64 s[2:3], s[2:3], 7
	s_add_u32 s20, s17, s2
	s_addc_u32 s21, s25, s3
	v_readfirstlane_b32 s19, v162
	v_lshl_add_u64 v[232:233], s[20:21], 0, v[142:143]
	s_mov_b32 m0, s19
	v_readfirstlane_b32 s19, v175
	global_load_lds_dwordx4 v[232:233], off
	v_lshl_add_u64 v[232:233], s[20:21], 0, v[144:145]
	s_mov_b32 m0, s19
	s_nop 0
	global_load_lds_dwordx4 v[232:233], off
	s_add_u32 s20, s4, s2
	s_addc_u32 s21, s5, s3
	v_readfirstlane_b32 s19, v1
	v_lshl_add_u64 v[232:233], s[20:21], 0, v[146:147]
	s_mov_b32 m0, s19
	v_readfirstlane_b32 s19, v176
	global_load_lds_dwordx4 v[232:233], off
	v_lshl_add_u64 v[232:233], s[20:21], 0, v[148:149]
	s_mov_b32 m0, s19
	s_nop 0
	global_load_lds_dwordx4 v[232:233], off
	s_add_u32 s20, s6, s2
	s_addc_u32 s21, s7, s3
	v_readfirstlane_b32 s19, v163
	v_lshl_add_u64 v[232:233], s[20:21], 0, v[142:143]
	s_mov_b32 m0, s19
	v_readfirstlane_b32 s19, v177
	global_load_lds_dwordx4 v[232:233], off
	v_lshl_add_u64 v[232:233], s[20:21], 0, v[144:145]
	s_mov_b32 m0, s19
	s_nop 0
	global_load_lds_dwordx4 v[232:233], off
	s_waitcnt vmcnt(6)
	s_waitcnt lgkmcnt(0)
	s_barrier
	s_setprio 1
	v_mfma_f32_16x16x32_f16 v[62:65], v[130:133], v[184:187], v[62:65]
	v_mfma_f32_16x16x32_f16 v[58:61], v[150:153], v[184:187], v[58:61]
	v_mfma_f32_16x16x32_f16 v[54:57], v[130:133], v[192:195], v[54:57]
	v_mfma_f32_16x16x32_f16 v[50:53], v[150:153], v[192:195], v[50:53]
	v_mfma_f32_16x16x32_f16 v[46:49], v[130:133], v[200:203], v[46:49]
	v_mfma_f32_16x16x32_f16 v[42:45], v[150:153], v[200:203], v[42:45]
	v_mfma_f32_16x16x32_f16 v[38:41], v[130:133], v[208:211], v[38:41]
	v_mfma_f32_16x16x32_f16 v[34:37], v[150:153], v[208:211], v[34:37]
	v_mfma_f32_16x16x32_f16 v[62:65], v[134:137], v[188:191], v[62:65]
	v_mfma_f32_16x16x32_f16 v[58:61], v[154:157], v[188:191], v[58:61]
	v_mfma_f32_16x16x32_f16 v[54:57], v[134:137], v[196:199], v[54:57]
	v_mfma_f32_16x16x32_f16 v[50:53], v[154:157], v[196:199], v[50:53]
	v_mfma_f32_16x16x32_f16 v[46:49], v[134:137], v[204:207], v[46:49]
	v_mfma_f32_16x16x32_f16 v[42:45], v[154:157], v[204:207], v[42:45]
	v_mfma_f32_16x16x32_f16 v[38:41], v[134:137], v[212:215], v[38:41]
	v_mfma_f32_16x16x32_f16 v[34:37], v[154:157], v[212:215], v[34:37]
	v_mfma_f32_16x16x32_f16 v[30:33], v[216:219], v[184:187], v[30:33]
	v_mfma_f32_16x16x32_f16 v[26:29], v[224:227], v[184:187], v[26:29]
	v_mfma_f32_16x16x32_f16 v[22:25], v[216:219], v[192:195], v[22:25]
	v_mfma_f32_16x16x32_f16 v[18:21], v[224:227], v[192:195], v[18:21]
	v_mfma_f32_16x16x32_f16 v[14:17], v[216:219], v[200:203], v[14:17]
	v_mfma_f32_16x16x32_f16 v[10:13], v[224:227], v[200:203], v[10:13]
	v_mfma_f32_16x16x32_f16 v[6:9], v[216:219], v[208:211], v[6:9]
	v_mfma_f32_16x16x32_f16 v[2:5], v[224:227], v[208:211], v[2:5]
	v_mfma_f32_16x16x32_f16 v[30:33], v[220:223], v[188:191], v[30:33]
	v_mfma_f32_16x16x32_f16 v[26:29], v[228:231], v[188:191], v[26:29]
	v_mfma_f32_16x16x32_f16 v[22:25], v[220:223], v[196:199], v[22:25]
	v_mfma_f32_16x16x32_f16 v[18:21], v[228:231], v[196:199], v[18:21]
	v_mfma_f32_16x16x32_f16 v[14:17], v[220:223], v[204:207], v[14:17]
	v_mfma_f32_16x16x32_f16 v[10:13], v[228:231], v[204:207], v[10:13]
	v_mfma_f32_16x16x32_f16 v[6:9], v[220:223], v[212:215], v[6:9]
	v_mfma_f32_16x16x32_f16 v[2:5], v[228:231], v[212:215], v[2:5]
	s_setprio 0
	s_barrier
	ds_read_b128 v[130:133], v159
	ds_read_b128 v[134:137], v159 offset:1024
	ds_read_b128 v[150:153], v159 offset:2048
	ds_read_b128 v[154:157], v159 offset:3072
	s_add_u32 s2, s10, s2
	s_addc_u32 s3, s16, s3
	v_readfirstlane_b32 s19, v178
	v_lshl_add_u64 v[216:217], s[2:3], 0, v[146:147]
	s_mov_b32 m0, s19
	ds_read_b128 v[184:187], v169 offset:32768
	ds_read_b128 v[188:191], v169 offset:33792
	ds_read_b128 v[192:195], v170 offset:32768
	ds_read_b128 v[196:199], v170 offset:33792
	ds_read_b128 v[200:203], v171 offset:32768
	ds_read_b128 v[204:207], v171 offset:33792
	ds_read_b128 v[208:211], v172 offset:32768
	ds_read_b128 v[212:215], v172 offset:33792
	global_load_lds_dwordx4 v[216:217], off
	v_lshl_add_u64 v[216:217], s[2:3], 0, v[148:149]
	v_readfirstlane_b32 s2, v179
	s_mov_b32 m0, s2
	s_nop 0
	global_load_lds_dwordx4 v[216:217], off
	ds_read_b128 v[216:219], v158
	ds_read_b128 v[220:223], v158 offset:1024
	ds_read_b128 v[224:227], v158 offset:2048
	ds_read_b128 v[228:231], v158 offset:3072
	s_waitcnt lgkmcnt(0)
	s_barrier
	s_setprio 1
	v_mfma_f32_16x16x32_f16 v[122:125], v[130:133], v[184:187], v[122:125]
	v_mfma_f32_16x16x32_f16 v[126:129], v[150:153], v[184:187], v[126:129]
	v_mfma_f32_16x16x32_f16 v[118:121], v[130:133], v[192:195], v[118:121]
	v_mfma_f32_16x16x32_f16 v[114:117], v[150:153], v[192:195], v[114:117]
	v_mfma_f32_16x16x32_f16 v[110:113], v[130:133], v[200:203], v[110:113]
	v_mfma_f32_16x16x32_f16 v[106:109], v[150:153], v[200:203], v[106:109]
	v_mfma_f32_16x16x32_f16 v[102:105], v[130:133], v[208:211], v[102:105]
	v_mfma_f32_16x16x32_f16 v[98:101], v[150:153], v[208:211], v[98:101]
	v_mfma_f32_16x16x32_f16 v[122:125], v[134:137], v[188:191], v[122:125]
	v_mfma_f32_16x16x32_f16 v[126:129], v[154:157], v[188:191], v[126:129]
	v_mfma_f32_16x16x32_f16 v[118:121], v[134:137], v[196:199], v[118:121]
	v_mfma_f32_16x16x32_f16 v[114:117], v[154:157], v[196:199], v[114:117]
	v_mfma_f32_16x16x32_f16 v[110:113], v[134:137], v[204:207], v[110:113]
	v_mfma_f32_16x16x32_f16 v[106:109], v[154:157], v[204:207], v[106:109]
	v_mfma_f32_16x16x32_f16 v[102:105], v[134:137], v[212:215], v[102:105]
	v_mfma_f32_16x16x32_f16 v[98:101], v[154:157], v[212:215], v[98:101]
	v_mfma_f32_16x16x32_f16 v[94:97], v[216:219], v[184:187], v[94:97]
	v_mfma_f32_16x16x32_f16 v[90:93], v[224:227], v[184:187], v[90:93]
	v_mfma_f32_16x16x32_f16 v[86:89], v[216:219], v[192:195], v[86:89]
	v_mfma_f32_16x16x32_f16 v[82:85], v[224:227], v[192:195], v[82:85]
	v_mfma_f32_16x16x32_f16 v[78:81], v[216:219], v[200:203], v[78:81]
	v_mfma_f32_16x16x32_f16 v[74:77], v[224:227], v[200:203], v[74:77]
	v_mfma_f32_16x16x32_f16 v[70:73], v[216:219], v[208:211], v[70:73]
	v_mfma_f32_16x16x32_f16 v[66:69], v[224:227], v[208:211], v[66:69]
	v_mfma_f32_16x16x32_f16 v[94:97], v[220:223], v[188:191], v[94:97]
	v_mfma_f32_16x16x32_f16 v[90:93], v[228:231], v[188:191], v[90:93]
	v_mfma_f32_16x16x32_f16 v[86:89], v[220:223], v[196:199], v[86:89]
	v_mfma_f32_16x16x32_f16 v[82:85], v[228:231], v[196:199], v[82:85]
	v_mfma_f32_16x16x32_f16 v[78:81], v[220:223], v[204:207], v[78:81]
	v_mfma_f32_16x16x32_f16 v[74:77], v[228:231], v[204:207], v[74:77]
	v_mfma_f32_16x16x32_f16 v[70:73], v[220:223], v[212:215], v[70:73]
	v_mfma_f32_16x16x32_f16 v[66:69], v[228:231], v[212:215], v[66:69]
	s_setprio 0
	s_barrier
	ds_read_b128 v[184:187], v169 offset:49152
	ds_read_b128 v[188:191], v169 offset:50176
	ds_read_b128 v[192:195], v170 offset:49152
	ds_read_b128 v[196:199], v170 offset:50176
	ds_read_b128 v[200:203], v171 offset:49152
	ds_read_b128 v[204:207], v171 offset:50176
	ds_read_b128 v[208:211], v172 offset:49152
	ds_read_b128 v[212:215], v172 offset:50176
	s_add_i32 s2, s18, 3
	s_ashr_i32 s3, s2, 31
	s_lshl_b64 s[2:3], s[2:3], 7
	s_add_u32 s18, s17, s2
	s_addc_u32 s19, s25, s3
	v_readfirstlane_b32 s20, v164
	v_lshl_add_u64 v[232:233], s[18:19], 0, v[142:143]
	s_mov_b32 m0, s20
	s_nop 0
	global_load_lds_dwordx4 v[232:233], off
	v_lshl_add_u64 v[232:233], s[18:19], 0, v[144:145]
	v_readfirstlane_b32 s18, v180
	s_mov_b32 m0, s18
	s_nop 0
	global_load_lds_dwordx4 v[232:233], off
	s_add_u32 s18, s4, s2
	s_addc_u32 s19, s5, s3
	v_readfirstlane_b32 s20, v181
	v_lshl_add_u64 v[232:233], s[18:19], 0, v[146:147]
	s_mov_b32 m0, s20
	s_nop 0
	global_load_lds_dwordx4 v[232:233], off
	v_lshl_add_u64 v[232:233], s[18:19], 0, v[148:149]
	v_readfirstlane_b32 s18, v182
	s_mov_b32 m0, s18
	s_nop 0
	global_load_lds_dwordx4 v[232:233], off
	s_add_u32 s2, s6, s2
	s_addc_u32 s3, s7, s3
	v_readfirstlane_b32 s18, v165
	v_lshl_add_u64 v[232:233], s[2:3], 0, v[142:143]
	s_mov_b32 m0, s18
	s_nop 0
	global_load_lds_dwordx4 v[232:233], off
	v_lshl_add_u64 v[232:233], s[2:3], 0, v[144:145]
	v_readfirstlane_b32 s2, v183
	s_mov_b32 m0, s2
	s_nop 0
	global_load_lds_dwordx4 v[232:233], off
	s_waitcnt vmcnt(6)
	s_waitcnt lgkmcnt(0)
	s_barrier
	s_setprio 1
	v_mfma_f32_16x16x32_f16 v[62:65], v[130:133], v[184:187], v[62:65]
	v_mfma_f32_16x16x32_f16 v[58:61], v[150:153], v[184:187], v[58:61]
	v_mfma_f32_16x16x32_f16 v[54:57], v[130:133], v[192:195], v[54:57]
	v_mfma_f32_16x16x32_f16 v[50:53], v[150:153], v[192:195], v[50:53]
	v_mfma_f32_16x16x32_f16 v[46:49], v[130:133], v[200:203], v[46:49]
	v_mfma_f32_16x16x32_f16 v[42:45], v[150:153], v[200:203], v[42:45]
	v_mfma_f32_16x16x32_f16 v[38:41], v[130:133], v[208:211], v[38:41]
	v_mfma_f32_16x16x32_f16 v[34:37], v[150:153], v[208:211], v[34:37]
	v_mfma_f32_16x16x32_f16 v[62:65], v[134:137], v[188:191], v[62:65]
	v_mfma_f32_16x16x32_f16 v[58:61], v[154:157], v[188:191], v[58:61]
	v_mfma_f32_16x16x32_f16 v[54:57], v[134:137], v[196:199], v[54:57]
	v_mfma_f32_16x16x32_f16 v[50:53], v[154:157], v[196:199], v[50:53]
	v_mfma_f32_16x16x32_f16 v[46:49], v[134:137], v[204:207], v[46:49]
	v_mfma_f32_16x16x32_f16 v[42:45], v[154:157], v[204:207], v[42:45]
	v_mfma_f32_16x16x32_f16 v[38:41], v[134:137], v[212:215], v[38:41]
	v_mfma_f32_16x16x32_f16 v[34:37], v[154:157], v[212:215], v[34:37]
	v_mfma_f32_16x16x32_f16 v[30:33], v[216:219], v[184:187], v[30:33]
	v_mfma_f32_16x16x32_f16 v[26:29], v[224:227], v[184:187], v[26:29]
	v_mfma_f32_16x16x32_f16 v[22:25], v[216:219], v[192:195], v[22:25]
	v_mfma_f32_16x16x32_f16 v[18:21], v[224:227], v[192:195], v[18:21]
	v_mfma_f32_16x16x32_f16 v[14:17], v[216:219], v[200:203], v[14:17]
	v_mfma_f32_16x16x32_f16 v[10:13], v[224:227], v[200:203], v[10:13]
	v_mfma_f32_16x16x32_f16 v[6:9], v[216:219], v[208:211], v[6:9]
	v_mfma_f32_16x16x32_f16 v[2:5], v[224:227], v[208:211], v[2:5]
	v_mfma_f32_16x16x32_f16 v[30:33], v[220:223], v[188:191], v[30:33]
	v_mfma_f32_16x16x32_f16 v[26:29], v[228:231], v[188:191], v[26:29]
	v_mfma_f32_16x16x32_f16 v[22:25], v[220:223], v[196:199], v[22:25]
	v_mfma_f32_16x16x32_f16 v[18:21], v[228:231], v[196:199], v[18:21]
	v_mfma_f32_16x16x32_f16 v[14:17], v[220:223], v[204:207], v[14:17]
	v_mfma_f32_16x16x32_f16 v[10:13], v[228:231], v[204:207], v[10:13]
	v_mfma_f32_16x16x32_f16 v[6:9], v[220:223], v[212:215], v[6:9]
	v_mfma_f32_16x16x32_f16 v[2:5], v[228:231], v[212:215], v[2:5]
	s_setprio 0
	s_cmp_lt_i32 s26, s24
	s_barrier
	s_cbranch_scc1 .LBB7_11
